# combo8 = combo7 + second slot atomic issued with the first + barrier followers invalidate on arrival
# baseline (speedup 1.0000x reference)
.LBB0_93:
	s_or_b64 exec, exec, s[12:13]
	v_cvt_f32_u32_e32 v5, v3
	s_waitcnt vmcnt(0)
	v_readfirstlane_b32 s10, v4
	v_sub_u32_e32 v4, 0, v3
	v_rcp_iflag_f32_e32 v5, v5
	v_add_u32_e32 v6, s10, v2
	v_mul_f32_e32 v5, 0x4f7ffffe, v5
	v_cvt_u32_f32_e32 v5, v5
	v_mul_lo_u32 v2, v4, v5
	v_mul_hi_u32 v2, v5, v2
	v_add_u32_e32 v2, v5, v2
	v_mul_hi_u32 v2, v6, v2
	v_mul_lo_u32 v4, v2, v3
	v_sub_u32_e32 v4, v6, v4
	v_add_u32_e32 v5, 1, v2
	v_cmp_ge_u32_e32 vcc, v4, v3
	s_nop 1
	v_cndmask_b32_e32 v2, v2, v5, vcc
	v_sub_u32_e32 v5, v4, v3
	v_cndmask_b32_e32 v4, v4, v5, vcc
	v_add_u32_e32 v5, 1, v2
	v_cmp_ge_u32_e32 vcc, v4, v3
	v_add_u32_e32 v4, 1, v6
	s_nop 0
	v_cndmask_b32_e32 v2, v2, v5, vcc
	v_mul_lo_u32 v5, v3, v2
	v_add_u32_e32 v3, v5, v3
	v_cmp_ne_u32_e32 vcc, v4, v3
	s_and_saveexec_b64 s[10:11], vcc
	s_xor_b64 s[10:11], exec, s[10:11]
	s_cbranch_execz .LBB0_107
	s_waitcnt lgkmcnt(0)
	buffer_inv sc1
	v_mov_b32_e32 v1, 0x2000
	global_load_dword v1, v1, s[8:9] offset:1024 sc1
	s_add_u32 s14, s8, 0x2400
	s_addc_u32 s15, s9, 0
	s_waitcnt vmcnt(0)
	v_cmp_eq_u32_e32 vcc, v1, v2
	s_and_saveexec_b64 s[12:13], vcc
	s_cbranch_execz .LBB0_106
	s_mov_b32 s26, 1
	s_mov_b64 s[16:17], 0
	v_mov_b32_e32 v1, 0
	s_branch .LBB0_97

.LBB0_106:
	s_or_b64 exec, exec, s[12:13]
	s_waitcnt vmcnt(0)
	s_waitcnt vmcnt(0)

.LBB0_908:
	s_or_b64 exec, exec, s[10:11]
	v_add_u32_e32 v18, v3, v10
	v_mov_b32_e32 v19, v127
	v_lshl_add_u64 v[20:21], v[18:19], 2, s[26:27]
	global_atomic_add v11, v[20:21], v162, off sc0
	v_cndmask_b32_e32 v16, v16, v5, vcc
	v_sub_f32_e32 v6, v6, v2
	v_add_u32_e32 v2, v7, v10
	v_sub_f32_e32 v7, v12, v16
	v_sub_f32_e32 v12, v8, v16
	v_sub_f32_e32 v10, v13, v16
	v_sub_f32_e32 v13, v9, v16
	v_or_b32_e32 v17, s78, v0
	v_mov_b32_e32 v3, v127
	v_sub_f32_e32 v14, v14, v16
	v_sub_f32_e32 v15, v15, v16
	v_sub_f32_e32 v19, v4, v16
	v_sub_f32_e32 v16, v5, v16
	v_lshl_add_u64 v[4:5], v[2:3], 2, s[26:27]
	global_atomic_add v3, v[4:5], v162, off sc0
	v_mul_f32_e32 v20, 0x3fb8aa3b, v6
	v_lshlrev_b32_e32 v6, 1, v17
	s_waitcnt vmcnt(1)
	v_lshl_add_u32 v8, v18, 14, v11
	v_ashrrev_i32_e32 v9, 31, v8
	v_lshl_add_u64 v[8:9], v[8:9], 2, s[18:19]
	global_store_dword v[8:9], v17, off
	v_mul_f32_e32 v5, 0x3fb8aa3b, v7
	v_mul_f32_e32 v8, 0x3fb8aa3b, v10
	v_mul_f32_e32 v9, 0x3fb8aa3b, v12
	v_mul_f32_e32 v12, 0x3fb8aa3b, v14
	v_mul_f32_e32 v14, 0x3fb8aa3b, v19
	v_exp_f32_e32 v19, v5
	v_mul_f32_e32 v10, 0x3fb8aa3b, v13
	v_mul_f32_e32 v13, 0x3fb8aa3b, v15
	v_mul_f32_e32 v15, 0x3fb8aa3b, v16
	v_exp_f32_e32 v16, v20
	v_exp_f32_e32 v20, v8
	v_exp_f32_e32 v21, v9
	v_exp_f32_e32 v10, v10
	v_exp_f32_e32 v12, v12
	v_add_f32_e32 v19, 0, v19
	v_exp_f32_e32 v13, v13
	v_add_f32_e32 v19, v20, v19
	v_exp_f32_e32 v14, v14
	v_add_f32_e32 v22, 1.0, v16
	v_add_f32_e32 v19, v21, v19
	v_exp_f32_e32 v15, v15
	v_div_scale_f32 v23, s[8:9], v22, v22, 1.0
	v_add_f32_e32 v10, v10, v19
	v_rcp_f32_e32 v20, v23
	v_add_f32_e32 v10, v12, v10
	v_add_f32_e32 v10, v13, v10
	v_add_f32_e32 v10, v14, v10
	v_add_f32_e32 v10, v15, v10
	v_fma_f32 v12, -v23, v20, 1.0
	v_div_scale_f32 v14, s[46:47], v10, v10, 1.0
	v_div_scale_f32 v24, s[8:9], 1.0, v22, 1.0
	v_fmac_f32_e32 v20, v12, v20
	v_rcp_f32_e32 v28, v14
	v_mul_f32_e32 v12, v24, v20
	v_fma_f32 v19, -v23, v12, v24
	v_div_scale_f32 v25, s[10:11], v22, v22, v16
	v_fmac_f32_e32 v12, v19, v20
	v_rcp_f32_e32 v27, v25
	v_fma_f32 v19, -v23, v12, v24
	v_fma_f32 v23, -v14, v28, 1.0
	v_div_scale_f32 v15, vcc, 1.0, v10, 1.0
	v_fmac_f32_e32 v28, v23, v28
	v_mul_f32_e32 v23, v15, v28
	v_fma_f32 v24, -v14, v23, v15
	v_fma_f32 v13, -v25, v27, 1.0
	v_fmac_f32_e32 v23, v24, v28
	v_div_scale_f32 v26, s[10:11], v16, v22, v16
	v_fmac_f32_e32 v27, v13, v27
	v_fma_f32 v14, -v14, v23, v15
	v_mul_f32_e32 v13, v26, v27
	v_div_fmas_f32 v14, v14, v28, v23
	s_mov_b64 vcc, s[8:9]
	v_ashrrev_i32_e32 v7, 31, v6
	v_fma_f32 v21, -v25, v13, v26
	v_div_fmas_f32 v12, v19, v20, v12
	v_or_b32_e32 v4, 1, v6
	v_lshlrev_b64 v[6:7], 2, v[6:7]
	v_fmac_f32_e32 v13, v21, v27
	v_div_fixup_f32 v10, v14, v10, 1.0
	v_div_fixup_f32 v12, v12, v22, 1.0
	v_lshl_add_u64 v[8:9], s[20:21], 0, v[6:7]
	v_lshl_add_u64 v[6:7], s[22:23], 0, v[6:7]
	v_fma_f32 v21, -v25, v13, v26
	s_mov_b64 vcc, s[10:11]
	v_mul_f32_e32 v12, v10, v12
	v_div_fmas_f32 v13, v21, v27, v13
	global_store_dword v[6:7], v12, off
	v_div_fixup_f32 v13, v13, v22, v16
	v_ashrrev_i32_e32 v5, 31, v4
	v_mul_f32_e32 v13, v10, v13
	v_lshl_or_b32 v10, v18, 16, v11
	v_lshl_add_u64 v[4:5], v[4:5], 2, s[22:23]
	s_waitcnt vmcnt(2)
	v_lshl_add_u32 v6, v2, 14, v3
	v_ashrrev_i32_e32 v7, 31, v6
	v_lshl_or_b32 v11, v2, 16, v3
	v_lshl_add_u64 v[2:3], v[6:7], 2, s[18:19]
	global_store_dword v[2:3], v17, off
	global_store_dwordx2 v[8:9], v[10:11], off
	global_store_dword v[4:5], v13, off
